# speedup vs baseline: 1.0083x; 1.0083x over previous
.Lm_flush:
	s_nop 5
	v_div_scale_f32 v132, s[30:31], v42, v42, 1.0
	v_rcp_f32_e32 v133, v132
	v_div_scale_f32 v134, vcc, 1.0, v42, 1.0
	v_fma_f32 v135, -v132, v133, 1.0
	v_fmac_f32_e32 v133, v135, v133
	v_mul_f32_e32 v135, v134, v133
	v_fma_f32 v136, -v132, v135, v134
	v_fmac_f32_e32 v135, v136, v133
	v_fma_f32 v132, -v132, v135, v134
	s_mul_i32 s40, s29, 0x180
	s_lshl_b32 s41, s18, 5
	v_div_fmas_f32 v132, v132, v133, v135
	v_div_fixup_f32 v132, v132, v42, 1.0
	v_cmp_lt_f32_e32 vcc, 0, v42
	s_add_u32 s40, s40, s41
	s_lshl_b32 s44, s40, 2
	s_mul_i32 s45, s40, 0x68
	s_add_u32 s42, s16, s44
	s_addc_u32 s43, s17, 0
	v_cndmask_b32_e32 v130, 0, v132, vcc
	s_add_u32 s40, s14, s45
	s_addc_u32 s41, s15, 0
	v_mov_b32_e32 v131, v130
	v_pk_mul_f32 v[132:133], v[16:17], v[130:131]
	v_pk_mul_f32 v[134:135], v[18:19], v[130:131]
	v_cvt_pk_f16_f32 v136, v132, v133
	v_cvt_pk_f16_f32 v137, v134, v135
	ds_write_b64 v6, v[136:137] offset:0
	v_pk_mul_f32 v[132:133], v[20:21], v[130:131]
	v_pk_mul_f32 v[134:135], v[22:23], v[130:131]
	v_cvt_pk_f16_f32 v136, v132, v133
	v_cvt_pk_f16_f32 v137, v134, v135
	ds_write_b64 v6, v[136:137] offset:16
	v_pk_mul_f32 v[132:133], v[24:25], v[130:131]
	v_pk_mul_f32 v[134:135], v[26:27], v[130:131]
	v_cvt_pk_f16_f32 v136, v132, v133
	v_cvt_pk_f16_f32 v137, v134, v135
	ds_write_b64 v6, v[136:137] offset:32
	v_pk_mul_f32 v[132:133], v[28:29], v[130:131]
	v_pk_mul_f32 v[134:135], v[30:31], v[130:131]
	v_cvt_pk_f16_f32 v136, v132, v133
	v_cvt_pk_f16_f32 v137, v134, v135
	ds_write_b64 v6, v[136:137] offset:48
	v_pk_mul_f32 v[132:133], v[32:33], v[130:131]
	v_pk_mul_f32 v[134:135], v[34:35], v[130:131]
	v_cvt_pk_f16_f32 v136, v132, v133
	v_cvt_pk_f16_f32 v137, v134, v135
	ds_write_b64 v6, v[136:137] offset:64
	v_pk_mul_f32 v[132:133], v[36:37], v[130:131]
	v_pk_mul_f32 v[134:135], v[38:39], v[130:131]
	v_cvt_pk_f16_f32 v136, v132, v133
	v_cvt_pk_f16_f32 v137, v134, v135
	ds_write_b64 v6, v[136:137] offset:80
	s_mov_b32 exec_hi, 0
	v_pk_mul_f32 v[132:133], v[40:41], v[130:131]
	v_pk_mul_f32 v[134:135], v[42:43], v[130:131]
	v_cvt_pk_f16_f32 v136, v132, v133
	v_cvt_pk_f16_f32 v137, v134, v135
	ds_write_b64 v6, v[136:137] offset:96
	s_mov_b64 exec, -1
	ds_read_b128 v[132:135], v7 offset:0
	ds_read_b128 v[136:139], v7 offset:1024
	ds_read_b128 v[140:143], v7 offset:2048
	ds_read_b128 v[144:147], v7 offset:3072
	v_log_f32_e32 v131, v42
	s_waitcnt lgkmcnt(0)
	v_sub_f32_e32 v131, v131, v148
	global_store_dwordx4 v2, v[132:135], s[40:41] offset:0 nt
	global_store_dwordx4 v2, v[136:139], s[40:41] offset:1024 nt
	global_store_dwordx4 v2, v[140:143], s[40:41] offset:2048 nt
	v_cndmask_b32_e32 v131, v150, v131, vcc
	s_mov_b32 exec_lo, 0xffff
	s_mov_b32 exec_hi, 0
	global_store_dwordx4 v2, v[144:147], s[40:41] offset:3072 nt
	s_mov_b32 exec_lo, -1
	global_store_dword v5, v131, s[42:43]
	s_mov_b64 exec, -1
	s_cmp_lt_u32 s27, 9
	s_cbranch_scc1 .Lm_switch
	s_endpgm
